# mLSTM gate scans on wave 0: DPP row-shift/broadcast scans instead of 12 ds_bpermute round trips per item
# speedup vs baseline: 1.0058x; 1.0046x over previous
; #define LAS __attribute__((address_space(3)))
; __device__ __forceinline__ float logsigmoid(float x) { return fminf(x, 0.f) - log1pf(__expf(-fabsf(x))); }
; __device__ __forceinline__ void p2_mlstm_local(const Params& P, LAS unsigned char* lds, int tid, int lane, int wave, int vb) {
;     ...
;         const P2Raw cur = pre;
; #pragma unroll
;         for (int i = 0; i < 5; ++i) { const int v = tid + 512 * i; if (v < 2144) *(LAS v4u*)(RAW + (v >> 5) * 512 + (v & 31) * 16) = cur.raw[i]; }
;         if (wave == 0) {
;             const float lf = logsigmoid(cur.lfi), ip = cur.ipi;
;             const float bc = scan_add(lf, lane), gg = __shfl(bc, 63), ds = gg - bc + ip, ml = wave_max(ds);
;             sw[lane] = __expf(ds - ml);
;             if (lane == 0) { SC[item] = ml; SC[2048 + item] = gg; }
;         }
.LBB0_467:
	s_waitcnt vmcnt(2)
	ds_write_b128 v57, v[52:55] offset:40960
	s_waitcnt vmcnt(1)
	ds_write_b128 v58, v[2:5] offset:40960
	s_waitcnt vmcnt(0)
	ds_write_b128 v57, v[6:9] offset:57344
	s_and_saveexec_b64 s[24:25], s[18:19]
	ds_write_b128 v59, v[14:17] offset:40960
	s_or_b64 exec, exec, s[24:25]
	s_and_saveexec_b64 s[24:25], s[20:21]
	ds_write_b128 v60, v[18:21] offset:40960
	s_or_b64 exec, exec, s[24:25]
	v_cndmask_b32_e64 v10, 0, 1, s[36:37]
	v_cmp_ne_u32_e64 s[24:25], 1, v10
	s_andn2_b64 vcc, exec, s[36:37]
	s_cbranch_vccnz .LBB0_475
	v_mul_f32_e64 v10, |v38|, s61
	v_exp_f32_e32 v10, v10
	v_max_f32_e32 v12, v38, v38
	v_min_f32_e32 v22, 0, v12
	v_add_f32_e32 v23, 1.0, v10
	v_add_f32_e32 v12, -1.0, v23
	v_sub_f32_e32 v13, v12, v23
	v_sub_f32_e32 v12, v10, v12
	v_add_f32_e32 v13, 1.0, v13
	v_add_f32_e32 v24, v12, v13
	v_frexp_mant_f32_e32 v25, v23
	v_cvt_f64_f32_e32 v[12:13], v23
	v_frexp_exp_i32_f64_e32 v12, v[12:13]
	v_cmp_gt_f32_e32 vcc, s63, v25
	s_nop 1
	v_subbrev_co_u32_e32 v12, vcc, 0, v12, vcc
	v_sub_u32_e32 v13, 0, v12
	v_ldexp_f32 v23, v23, v13
	v_ldexp_f32 v13, v24, v13
	v_add_f32_e32 v24, -1.0, v23
	v_add_f32_e32 v27, 1.0, v23
	v_add_f32_e32 v25, 1.0, v24
	v_add_f32_e32 v28, -1.0, v27
	v_sub_f32_e32 v25, v23, v25
	v_sub_f32_e32 v23, v23, v28
	v_add_f32_e32 v25, v13, v25
	v_add_f32_e32 v13, v13, v23
	v_add_f32_e32 v23, v27, v13
	v_rcp_f32_e32 v28, v23
	v_add_f32_e32 v26, v24, v25
	v_sub_f32_e32 v24, v26, v24
	v_sub_f32_e32 v24, v25, v24
	v_sub_f32_e32 v25, v23, v27
	v_sub_f32_e32 v13, v13, v25
	v_mul_f32_e32 v25, v26, v28
	v_mul_f32_e32 v27, v23, v25
	v_fma_f32 v29, v25, v23, -v27
	v_fmac_f32_e32 v29, v25, v13
	v_add_f32_e32 v36, v27, v29
	v_sub_f32_e32 v37, v26, v36
	v_sub_f32_e32 v26, v26, v37
	v_sub_f32_e32 v27, v36, v27
	v_sub_f32_e32 v26, v26, v36
	v_add_f32_e32 v24, v24, v26
	v_sub_f32_e32 v26, v27, v29
	v_add_f32_e32 v24, v26, v24
	v_add_f32_e32 v26, v37, v24
	v_mul_f32_e32 v27, v28, v26
	v_mul_f32_e32 v29, v23, v27
	v_fma_f32 v23, v27, v23, -v29
	v_fmac_f32_e32 v23, v27, v13
	v_sub_f32_e32 v13, v37, v26
	v_add_f32_e32 v13, v24, v13
	v_add_f32_e32 v24, v29, v23
	v_sub_f32_e32 v36, v26, v24
	v_sub_f32_e32 v26, v26, v36
	v_sub_f32_e32 v29, v24, v29
	v_sub_f32_e32 v24, v26, v24
	v_add_f32_e32 v13, v13, v24
	v_sub_f32_e32 v23, v29, v23
	v_cvt_f32_i32_e32 v12, v12
	v_add_f32_e32 v13, v23, v13
	v_add_f32_e32 v23, v25, v27
	v_add_f32_e32 v13, v36, v13
	v_sub_f32_e32 v24, v23, v25
	v_mul_f32_e32 v13, v28, v13
	v_sub_f32_e32 v24, v27, v24
	v_add_f32_e32 v13, v24, v13
	v_mul_f32_e32 v27, 0x3f317218, v12
	v_add_f32_e32 v24, v23, v13
	v_fma_f32 v28, v12, s66, -v27
	v_mul_f32_e32 v25, v24, v24
	v_fmac_f32_e32 v28, 0xb102e308, v12
	v_sub_f32_e32 v12, v24, v23
	v_fmamk_f32 v26, v25, 0x3e9b6dac, v61
	v_sub_f32_e32 v12, v13, v12
	v_add_f32_e32 v13, v27, v28
	v_fmaak_f32 v26, v25, v26, 0x3f2aaada
	v_sub_f32_e32 v23, v13, v27
	v_ldexp_f32 v27, v24, 1
	v_mul_f32_e32 v24, v24, v25
	v_mul_f32_e32 v24, v24, v26
	v_add_f32_e32 v25, v27, v24
	v_sub_f32_e32 v26, v25, v27
	v_ldexp_f32 v12, v12, 1
	v_sub_f32_e32 v24, v24, v26
	v_add_f32_e32 v12, v12, v24
	v_add_f32_e32 v24, v25, v12
	v_sub_f32_e32 v25, v24, v25
	v_sub_f32_e32 v12, v12, v25
	v_add_f32_e32 v25, v13, v24
	v_sub_f32_e32 v26, v25, v13
	v_sub_f32_e32 v27, v25, v26
	v_sub_f32_e32 v23, v28, v23
	v_sub_f32_e32 v13, v13, v27
	v_sub_f32_e32 v24, v24, v26
	v_add_f32_e32 v13, v24, v13
	v_add_f32_e32 v24, v23, v12
	v_sub_f32_e32 v26, v24, v23
	v_sub_f32_e32 v27, v24, v26
	v_sub_f32_e32 v23, v23, v27
	v_sub_f32_e32 v12, v12, v26
	v_add_f32_e32 v13, v24, v13
	v_add_f32_e32 v12, v12, v23
	v_add_f32_e32 v23, v25, v13
	v_sub_f32_e32 v24, v23, v25
	v_sub_f32_e32 v13, v13, v24
	v_add_f32_e32 v12, v12, v13
	v_add_f32_e32 v12, v23, v12
	v_cmp_neq_f32_e32 vcc, s67, v10
	v_add_u32_e32 v13, -1, v69
	v_xor_b32_e32 v23, 2, v69
	v_cndmask_b32_e32 v12, v66, v12, vcc
	v_cmp_ngt_f32_e32 vcc, -1.0, v10
	s_nop 1
	v_cndmask_b32_e32 v12, v67, v12, vcc
	v_cmp_neq_f32_e32 vcc, -1.0, v10
	s_nop 1
	v_cndmask_b32_e32 v12, v68, v12, vcc
	v_cmp_lt_f32_e64 vcc, |v10|, s69
	s_nop 1
	v_cndmask_b32_e32 v10, v12, v10, vcc
	v_and_b32_e32 v12, 64, v69
	v_cmp_lt_i32_e32 vcc, v13, v12
	v_sub_f32_e32 v10, v22, v10
	v_xor_b32_e32 v22, 1, v69
	v_cndmask_b32_e32 v13, v13, v69, vcc
	v_lshlrev_b32_e32 v13, 2, v13
	s_nop 1
	v_add_f32_dpp v10, v10, v10 row_shr:1 row_mask:0xf bank_mask:0xf
	s_nop 1
	v_add_f32_dpp v10, v10, v10 row_shr:2 row_mask:0xf bank_mask:0xf
	s_nop 1
	v_add_f32_dpp v10, v10, v10 row_shr:4 row_mask:0xf bank_mask:0xf
	s_nop 1
	v_add_f32_dpp v10, v10, v10 row_shr:8 row_mask:0xf bank_mask:0xf
	s_nop 1
	v_add_f32_dpp v10, v10, v10 row_bcast:15 row_mask:0xa bank_mask:0xf
	s_nop 1
	v_add_f32_dpp v10, v10, v10 row_bcast:31 row_mask:0xc bank_mask:0xf
	v_mov_b32_e32 v13, v10
	s_nop 0
	v_readlane_b32 s98, v10, 63
	s_nop 1
	v_mov_b32_e32 v10, s98
	v_sub_f32_e32 v13, v10, v13
	v_add_f32_e32 v13, v39, v13
	v_mov_b32_e32 v22, v13
	s_nop 1
	v_max_f32_dpp v22, v22, v22 row_shr:1 row_mask:0xf bank_mask:0xf
	s_nop 1
	v_max_f32_dpp v22, v22, v22 row_shr:2 row_mask:0xf bank_mask:0xf
	s_nop 1
	v_max_f32_dpp v22, v22, v22 row_shr:4 row_mask:0xf bank_mask:0xf
	s_nop 1
	v_max_f32_dpp v22, v22, v22 row_shr:8 row_mask:0xf bank_mask:0xf
	s_nop 1
	v_max_f32_dpp v22, v22, v22 row_bcast:15 row_mask:0xa bank_mask:0xf
	s_nop 1
	v_max_f32_dpp v22, v22, v22 row_bcast:31 row_mask:0xc bank_mask:0xf
	s_nop 0
	v_readlane_b32 s98, v22, 63
	s_nop 1
	v_mov_b32_e32 v12, s98
	v_sub_f32_e32 v13, v13, v12
	v_mul_f32_e32 v13, 0x3fb8aa3b, v13
	v_exp_f32_e32 v13, v13
	ds_write_b32 v40, v13 offset:36864
	s_and_saveexec_b64 s[44:45], s[2:3]
	s_cbranch_execz .LBB0_474
	s_ashr_i32 s43, s42, 31
	s_lshl_b64 s[46:47], s[42:43], 2
	s_add_u32 s46, s55, s46
	s_addc_u32 s47, s57, s47
	global_store_dword v11, v12, s[46:47]
	global_store_dword v62, v10, s[46:47]

; __device__ __forceinline__ float logsigmoid(float x) { return fminf(x, 0.f) - log1pf(__expf(-fabsf(x))); }
; __device__ __forceinline__ void p4_mlstm_out(const Params& P, LAS unsigned char* lds, int tid, int lane, int wave, int vb) {
;     ...
;         if (wave == 0) {
;             const float lf = logsigmoid(pf.ifa), ip = pf.ifb;
;             const float bc = scan_add(lf, lane), a = ip - bc, pm = scan_max(a, lane), ms = SC[4096 + item], M = fmaxf(ms, pm);
;             sm[lane] = a; sm[64 + lane] = M; sm[128 + lane] = __expf(ms - M); sm[192 + lane] = __expf(-bc - M);
.LBB0_782:
	s_or_b64 exec, exec, s[56:57]
	v_cndmask_b32_e64 v46, 0, 1, s[78:79]
	v_cmp_ne_u32_e64 s[56:57], 1, v46
	s_andn2_b64 vcc, exec, s[78:79]
	v_mbcnt_hi_u32_b32 v72, -1, v241
	s_cbranch_vccnz .LBB0_784
	s_mov_b32 s0, 0xbfb8aa3b
	s_waitcnt vmcnt(11)
	v_mul_f32_e64 v46, |v171|, s0
	v_exp_f32_e32 v46, v46
	v_max_f32_e32 v52, v171, v171
	v_min_f32_e32 v54, 0, v52
	s_mov_b32 s0, 0x3f2aaaab
	v_add_f32_e32 v55, 1.0, v46
	v_add_f32_e32 v52, -1.0, v55
	v_sub_f32_e32 v53, v52, v55
	v_sub_f32_e32 v52, v46, v52
	v_add_f32_e32 v53, 1.0, v53
	v_add_f32_e32 v56, v52, v53
	v_frexp_mant_f32_e32 v57, v55
	v_cvt_f64_f32_e32 v[52:53], v55
	v_frexp_exp_i32_f64_e32 v52, v[52:53]
	v_cmp_gt_f32_e32 vcc, s0, v57
	s_mov_b32 s0, 0x3f317218
	s_ashr_i32 s85, s84, 31
	v_subbrev_co_u32_e32 v52, vcc, 0, v52, vcc
	v_sub_u32_e32 v53, 0, v52
	v_ldexp_f32 v55, v55, v53
	v_ldexp_f32 v53, v56, v53
	v_add_f32_e32 v56, -1.0, v55
	v_add_f32_e32 v59, 1.0, v55
	v_add_f32_e32 v57, 1.0, v56
	v_add_f32_e32 v60, -1.0, v59
	v_sub_f32_e32 v57, v55, v57
	v_sub_f32_e32 v55, v55, v60
	v_add_f32_e32 v57, v53, v57
	v_add_f32_e32 v53, v53, v55
	v_add_f32_e32 v55, v59, v53
	v_rcp_f32_e32 v60, v55
	v_add_f32_e32 v58, v56, v57
	v_sub_f32_e32 v56, v58, v56
	v_sub_f32_e32 v56, v57, v56
	v_sub_f32_e32 v57, v55, v59
	v_sub_f32_e32 v53, v53, v57
	v_mul_f32_e32 v57, v58, v60
	v_mul_f32_e32 v59, v55, v57
	v_fma_f32 v61, v57, v55, -v59
	v_fmac_f32_e32 v61, v57, v53
	v_add_f32_e32 v62, v59, v61
	v_sub_f32_e32 v63, v58, v62
	v_sub_f32_e32 v58, v58, v63
	v_sub_f32_e32 v59, v62, v59
	v_sub_f32_e32 v58, v58, v62
	v_add_f32_e32 v56, v56, v58
	v_sub_f32_e32 v58, v59, v61
	v_add_f32_e32 v56, v58, v56
	v_add_f32_e32 v58, v63, v56
	v_mul_f32_e32 v59, v60, v58
	v_mul_f32_e32 v61, v55, v59
	v_fma_f32 v55, v59, v55, -v61
	v_fmac_f32_e32 v55, v59, v53
	v_sub_f32_e32 v53, v63, v58
	v_add_f32_e32 v53, v56, v53
	v_add_f32_e32 v56, v61, v55
	v_sub_f32_e32 v62, v58, v56
	v_sub_f32_e32 v58, v58, v62
	v_sub_f32_e32 v61, v56, v61
	v_sub_f32_e32 v56, v58, v56
	v_add_f32_e32 v53, v53, v56
	v_sub_f32_e32 v55, v61, v55
	v_cvt_f32_i32_e32 v52, v52
	v_add_f32_e32 v53, v55, v53
	v_add_f32_e32 v55, v57, v59
	v_add_f32_e32 v53, v62, v53
	v_sub_f32_e32 v56, v55, v57
	v_mul_f32_e32 v53, v60, v53
	v_sub_f32_e32 v56, v59, v56
	v_add_f32_e32 v53, v56, v53
	v_mul_f32_e32 v59, 0x3f317218, v52
	v_add_f32_e32 v56, v55, v53
	v_fma_f32 v60, v52, s0, -v59
	v_mul_f32_e32 v57, v56, v56
	v_fmac_f32_e32 v60, 0xb102e308, v52
	v_sub_f32_e32 v52, v56, v55
	v_fmamk_f32 v58, v57, 0x3e9b6dac, v234
	v_sub_f32_e32 v52, v53, v52
	v_add_f32_e32 v53, v59, v60
	v_fmaak_f32 v58, v57, v58, 0x3f2aaada
	v_sub_f32_e32 v55, v53, v59
	v_ldexp_f32 v59, v56, 1
	v_mul_f32_e32 v56, v56, v57
	v_mul_f32_e32 v56, v56, v58
	v_add_f32_e32 v57, v59, v56
	v_sub_f32_e32 v58, v57, v59
	v_ldexp_f32 v52, v52, 1
	v_sub_f32_e32 v56, v56, v58
	v_add_f32_e32 v52, v52, v56
	v_add_f32_e32 v56, v57, v52
	v_sub_f32_e32 v57, v56, v57
	v_sub_f32_e32 v52, v52, v57
	v_add_f32_e32 v57, v53, v56
	v_sub_f32_e32 v58, v57, v53
	v_sub_f32_e32 v59, v57, v58
	v_sub_f32_e32 v55, v60, v55
	v_sub_f32_e32 v53, v53, v59
	v_sub_f32_e32 v56, v56, v58
	v_add_f32_e32 v53, v56, v53
	v_add_f32_e32 v56, v55, v52
	v_sub_f32_e32 v58, v56, v55
	v_sub_f32_e32 v59, v56, v58
	v_sub_f32_e32 v55, v55, v59
	v_sub_f32_e32 v52, v52, v58
	v_add_f32_e32 v53, v56, v53
	v_add_f32_e32 v52, v52, v55
	v_add_f32_e32 v55, v57, v53
	v_sub_f32_e32 v56, v55, v57
	v_sub_f32_e32 v53, v53, v56
	v_add_f32_e32 v52, v52, v53
	s_mov_b32 s0, 0x7f800000
	v_add_f32_e32 v52, v55, v52
	v_cmp_neq_f32_e32 vcc, s0, v46
	s_mov_b32 s0, 0x33800000
	v_add_u32_e32 v53, -1, v72
	v_cndmask_b32_e32 v52, v242, v52, vcc
	v_cmp_ngt_f32_e32 vcc, -1.0, v46
	s_lshl_b64 s[86:87], s[84:85], 2
	s_add_u32 s86, s64, s86
	v_cndmask_b32_e32 v52, v243, v52, vcc
	v_cmp_neq_f32_e32 vcc, -1.0, v46
	s_addc_u32 s87, s65, s87
	global_load_dword v57, v235, s[86:87]
	v_cndmask_b32_e32 v52, v244, v52, vcc
	v_cmp_lt_f32_e64 vcc, |v46|, s0
	s_nop 1
	v_cndmask_b32_e32 v46, v52, v46, vcc
	v_and_b32_e32 v52, 64, v72
	v_cmp_lt_i32_e32 vcc, v53, v52
	v_sub_f32_e32 v46, v54, v46
	s_nop 0
	v_cndmask_b32_e32 v53, v53, v72, vcc
	v_lshlrev_b32_e32 v53, 2, v53
	s_nop 1
	v_add_f32_dpp v46, v46, v46 row_shr:1 row_mask:0xf bank_mask:0xf
	s_nop 1
	v_add_f32_dpp v46, v46, v46 row_shr:2 row_mask:0xf bank_mask:0xf
	s_nop 1
	v_add_f32_dpp v46, v46, v46 row_shr:4 row_mask:0xf bank_mask:0xf
	s_nop 1
	v_add_f32_dpp v46, v46, v46 row_shr:8 row_mask:0xf bank_mask:0xf
	s_nop 1
	v_add_f32_dpp v46, v46, v46 row_bcast:15 row_mask:0xa bank_mask:0xf
	s_nop 1
	v_add_f32_dpp v46, v46, v46 row_bcast:31 row_mask:0xc bank_mask:0xf
	s_waitcnt vmcnt(11)
	v_sub_f32_e32 v59, v173, v46
	v_mov_b32_e32 v53, v59
	s_nop 1
	v_max_f32_dpp v53, v53, v53 row_shr:1 row_mask:0xf bank_mask:0xf
	s_nop 1
	v_max_f32_dpp v53, v53, v53 row_shr:2 row_mask:0xf bank_mask:0xf
	s_nop 1
	v_max_f32_dpp v53, v53, v53 row_shr:4 row_mask:0xf bank_mask:0xf
	s_nop 1
	v_max_f32_dpp v53, v53, v53 row_shr:8 row_mask:0xf bank_mask:0xf
	s_nop 1
	v_max_f32_dpp v53, v53, v53 row_bcast:15 row_mask:0xa bank_mask:0xf
	s_nop 1
	v_max_f32_dpp v53, v53, v53 row_bcast:31 row_mask:0xc bank_mask:0xf
	v_max_f32_e32 v52, v53, v53
	s_waitcnt vmcnt(0)
	v_max_f32_e32 v53, v57, v57
	v_max_f32_e32 v52, v53, v52
	v_sub_f32_e32 v53, v57, v52
	v_sub_f32_e64 v46, -v46, v52
	v_mul_f32_e32 v53, 0x3fb8aa3b, v53
	v_mul_f32_e32 v46, 0x3fb8aa3b, v46
	v_exp_f32_e32 v53, v53
	v_exp_f32_e32 v46, v46
	ds_write2st64_b32 v117, v59, v52 offset1:1
	ds_write2st64_b32 v117, v53, v46 offset0:2 offset1:3
